# stack + 10 expert-weight slices converted by idle workgroups of the two top-k phases instead of inside the scan
# speedup vs baseline: 1.0071x; 1.0015x over previous
.LBB0_422:
	s_ashr_i32 s11, s51, 16
	s_bfe_u32 s92, s51, 0x5000b
	v_readlane_b32 s76, v254, 36
	s_cmp_eq_u32 s11, 1
	v_readlane_b32 s77, v254, 37
	v_readlane_b32 s78, v254, 38
	v_readlane_b32 s79, v254, 39
	v_readlane_b32 s80, v254, 40
	v_readlane_b32 s81, v254, 41
	v_readlane_b32 s82, v254, 42
	v_readlane_b32 s83, v254, 43
	s_cselect_b32 s0, s76, s78
	s_cselect_b32 s1, s77, s79
	v_readlane_b32 s68, v254, 44
	s_cmp_lt_u32 s51, 0x10000
	v_readlane_b32 s82, v254, 58
	v_readlane_b32 s83, v254, 59
	s_cselect_b32 s1, s83, s1
	s_cselect_b32 s0, s82, s0
	s_lshl_b32 s12, s92, 24
	s_add_u32 s28, s0, s12
	s_addc_u32 s29, s1, 0
	v_readlane_b32 s69, v254, 45
	v_readlane_b32 s70, v254, 46
	v_readlane_b32 s71, v254, 47
	v_readlane_b32 s72, v254, 48
	v_readlane_b32 s73, v254, 49
	v_readlane_b32 s74, v254, 50
	v_readlane_b32 s75, v254, 51
	s_cmp_eq_u32 s92, 0
	s_cselect_b64 s[90:91], -1, 0
	v_readlane_b32 s60, v254, 20
	v_readlane_b32 s78, v254, 54
	v_readlane_b32 s79, v254, 55
	s_and_b64 s[0:1], s[90:91], exec
	v_readlane_b32 s74, v254, 34
	v_readlane_b32 s75, v254, 35
	s_cselect_b32 s30, s74, s78
	s_cselect_b32 s31, s75, s79
	s_cmp_eq_u32 s11, 3
	s_cselect_b64 s[52:53], -1, 0
	s_and_b64 s[0:1], s[52:53], exec
	s_cselect_b32 s1, s31, s29
	s_cselect_b32 s0, s30, s28
	s_and_b32 s43, s46, 0x7e0
	s_and_b32 s98, s51, 0x7c0
	s_lshl_b32 s98, s98, 13
	s_lshl_b32 s40, s43, 2
	s_add_u32 s98, s98, s40
	s_add_u32 s100, s0, s98
	s_addc_u32 s101, s1, 0
	global_load_dwordx4 v[152:155], v250, s[100:101]
	v_add_u32_e32 v253, 0x2000, v250
	global_load_dwordx4 v[156:159], v253, s[100:101]
	v_add_u32_e32 v252, 0x4000, v250
	global_load_dwordx4 v[160:163], v252, s[100:101]
	v_add_u32_e32 v253, 0x6000, v250
	global_load_dwordx4 v[164:167], v253, s[100:101]
	v_add_u32_e32 v252, 0x8000, v250
	global_load_dwordx4 v[168:171], v252, s[100:101]
	v_add_u32_e32 v253, 0xa000, v250
	global_load_dwordx4 v[172:175], v253, s[100:101]
	v_add_u32_e32 v252, 0xc000, v250
	global_load_dwordx4 v[176:179], v252, s[100:101]
	v_add_u32_e32 v253, 0xe000, v250
	global_load_dwordx4 v[246:249], v253, s[100:101]
	s_cmp_lt_u32 s7, 20
	s_cselect_b64 s[94:95], -1, 0
	s_and_b64 s[0:1], s[94:95], exec
	s_cselect_b32 s0, s49, 0
	s_add_i32 s0, s0, s44
	s_lshl_b32 s0, s0, 3
	v_readlane_b32 s1, v255, 15
	s_add_i32 s28, s1, s0
	s_cmp_gt_u32 s7, 11
	s_cselect_b32 s98, 0x5000, 0
	s_add_i32 s28, s28, s98
	s_bfe_u32 s93, s28, 0x5000b
	s_ashr_i32 s57, s28, 16
	s_lshl_b32 s13, s93, 22
	s_cmp_eq_u32 s57, 3
	s_cselect_b64 s[96:97], -1, 0
	s_cmp_eq_u32 s93, 0
	s_cselect_b64 s[0:1], -1, 0
	s_lshl_b32 s34, s28, 5
	s_and_b32 s37, s34, 0x7e0
	s_and_b32 s36, s28, 0x7c0
	s_mov_b32 s38, s86
	s_cmp_gt_u32 s7, 19
	v_readlane_b32 s76, v254, 52
	v_readlane_b32 s77, v254, 53
	v_readlane_b32 s80, v254, 56
	v_readlane_b32 s81, v254, 57
	v_readlane_b32 s61, v254, 21
	v_readlane_b32 s62, v254, 22
	v_readlane_b32 s63, v254, 23
	v_readlane_b32 s64, v254, 24
	v_readlane_b32 s65, v254, 25
	v_readlane_b32 s66, v254, 26
	v_readlane_b32 s67, v254, 27
	v_readlane_b32 s68, v254, 28
	v_readlane_b32 s69, v254, 29
	v_readlane_b32 s70, v254, 30
	v_readlane_b32 s71, v254, 31
	v_readlane_b32 s72, v254, 32
	v_readlane_b32 s73, v254, 33
	s_cbranch_scc1 .LBB0_424
	v_readlane_b32 s80, v254, 36
	s_cmp_eq_u32 s57, 1
	v_readlane_b32 s81, v254, 37
	v_readlane_b32 s82, v254, 38
	v_readlane_b32 s83, v254, 39
	s_cselect_b32 s29, s80, s82
	s_cselect_b32 s30, s81, s83
	v_readlane_b32 s68, v254, 44
	s_cmp_lt_u32 s28, 0x10000
	v_readlane_b32 s82, v254, 58
	v_readlane_b32 s83, v254, 59
	s_cselect_b32 s28, s83, s30
	s_cselect_b32 s29, s82, s29
	s_lshl_b32 s30, s13, 2
	v_readlane_b32 s69, v254, 45
	v_readlane_b32 s70, v254, 46
	v_readlane_b32 s71, v254, 47
	v_readlane_b32 s72, v254, 48
	v_readlane_b32 s73, v254, 49
	v_readlane_b32 s74, v254, 50
	v_readlane_b32 s75, v254, 51
	s_add_u32 s30, s29, s30
	s_addc_u32 s31, s28, 0
	v_readlane_b32 s60, v254, 20
	v_readlane_b32 s78, v254, 54
	v_readlane_b32 s79, v254, 55
	s_and_b64 s[28:29], s[0:1], exec
	v_readlane_b32 s74, v254, 34
	v_readlane_b32 s75, v254, 35
	s_cselect_b32 s60, s74, s78
	s_cselect_b32 vcc_lo, s75, s79
	s_and_b64 s[28:29], s[96:97], exec
	s_cselect_b32 s29, vcc_lo, s31
	s_cselect_b32 s28, s60, s30
	s_lshl_b32 s98, s36, 13
	s_lshl_b32 s40, s37, 2
	s_add_u32 s98, s98, s40
	s_add_u32 s100, s28, s98
	s_addc_u32 s101, s29, 0
	global_load_dwordx4 v[2:5], v250, s[100:101]
	v_add_u32_e32 v253, 0x2000, v250
	global_load_dwordx4 v[6:9], v253, s[100:101]
	v_add_u32_e32 v252, 0x4000, v250
	global_load_dwordx4 v[10:13], v252, s[100:101]
	v_add_u32_e32 v253, 0x6000, v250
	global_load_dwordx4 v[14:17], v253, s[100:101]
	v_add_u32_e32 v252, 0x8000, v250
	global_load_dwordx4 v[18:21], v252, s[100:101]
	v_add_u32_e32 v253, 0xa000, v250
	global_load_dwordx4 v[22:25], v253, s[100:101]
	v_add_u32_e32 v252, 0xc000, v250
	global_load_dwordx4 v[26:29], v252, s[100:101]
	v_add_u32_e32 v253, 0xe000, v250
	global_load_dwordx4 v[116:119], v253, s[100:101]
	v_readlane_b32 s84, v254, 40
	v_readlane_b32 s85, v254, 41
	v_readlane_b32 s86, v254, 42
	v_readlane_b32 s87, v254, 43
	v_readlane_b32 s76, v254, 52
	v_readlane_b32 s77, v254, 53
	v_readlane_b32 s80, v254, 56
	v_readlane_b32 s81, v254, 57
	v_readlane_b32 s61, v254, 21
	v_readlane_b32 s62, v254, 22
	v_readlane_b32 s63, v254, 23
	v_readlane_b32 s64, v254, 24
	v_readlane_b32 s65, v254, 25
	v_readlane_b32 s66, v254, 26
	v_readlane_b32 s67, v254, 27
	v_readlane_b32 s68, v254, 28
	v_readlane_b32 s69, v254, 29
	v_readlane_b32 s70, v254, 30
	v_readlane_b32 s71, v254, 31
	v_readlane_b32 s72, v254, 32
	v_readlane_b32 s73, v254, 33

.LBB0_858:
	s_or_b64 exec, exec, s[40:41]
	s_cmp_eq_u32 s68, 0
	s_cselect_b64 s[38:39], -1, 0
	s_and_b64 s[38:39], s[52:53], s[38:39]
	s_and_b64 s[40:41], s[38:39], s[36:37]
	s_and_saveexec_b64 s[38:39], s[40:41]
	s_cbranch_execz .LBB0_731
	v_add_lshl_u32 v2, v16, s73, 2
	v_lshl_or_b32 v3, s70, 7, v0
	global_store_dword v2, v3, s[46:47]
	global_store_dword v2, v7, s[48:49]
	s_branch .LBB0_731
	s_branch .LBB0_860
.Lhost_p8:
	s_sub_i32 s12, s85, 128
	s_lshr_b32 s13, s87, 6
	s_mul_i32 s12, s12, 64
	s_mul_i32 s13, s13, 8
	s_add_i32 s16, s12, s13
	v_readlane_b32 s8, v254, 38
	v_readlane_b32 s9, v254, 39
	v_readlane_b32 s10, v254, 42
	v_readlane_b32 s11, v254, 43
	v_lshrrev_b32_e32 v84, 3, v222
	v_and_b32_e32 v85, 7, v222
	v_lshlrev_b32_e32 v82, 16, v84
	v_lshlrev_b32_e32 v83, 4, v84
	v_lshl_or_b32 v82, v85, 4, v82
	v_lshl_or_b32 v83, v85, 9, v83
	s_add_u32 s10, s10, 0x24c00000
	s_addc_u32 s11, s11, 0
	s_mov_b32 s14, 4
.Lhost_p8_loop:
	s_lshr_b32 s17, s16, 11
	s_add_i32 s17, s17, 16
	s_and_b32 s18, s16, 2047
	s_lshr_b32 s19, s18, 6
	s_and_b32 s18, s18, 63
	s_lshl_b32 s20, s19, 19
	s_lshl_b32 s21, s18, 7
	s_add_i32 s20, s20, s21
	s_lshl_b32 s21, s17, 24
	s_add_u32 s20, s20, s21
	s_add_u32 s22, s8, s20
	s_addc_u32 s23, s9, 0
	s_lshl_b32 s21, s17, 23
	s_lshr_b32 s20, s18, 3
	s_lshl_b32 s20, s20, 20
	s_add_i32 s21, s21, s20
	s_lshl_b32 s20, s19, 15
	s_add_i32 s21, s21, s20
	s_and_b32 s20, s18, 7
	s_lshl_b32 s20, s20, 12
	s_add_i32 s21, s21, s20
	s_add_u32 s24, s10, s21
	s_addc_u32 s25, s11, 0
	s_add_i32 s15, s16, 1
	s_lshr_b32 s17, s15, 11
	s_add_i32 s17, s17, 16
	s_and_b32 s18, s15, 2047
	s_lshr_b32 s19, s18, 6
	s_and_b32 s18, s18, 63
	s_lshl_b32 s20, s19, 19
	s_lshl_b32 s21, s18, 7
	s_add_i32 s20, s20, s21
	s_lshl_b32 s21, s17, 24
	s_add_u32 s20, s20, s21
	s_add_u32 s26, s8, s20
	s_addc_u32 s27, s9, 0
	s_lshl_b32 s21, s17, 23
	s_lshr_b32 s20, s18, 3
	s_lshl_b32 s20, s20, 20
	s_add_i32 s21, s21, s20
	s_lshl_b32 s20, s19, 15
	s_add_i32 s21, s21, s20
	s_and_b32 s20, s18, 7
	s_lshl_b32 s20, s20, 12
	s_add_i32 s21, s21, s20
	s_add_u32 s28, s10, s21
	s_addc_u32 s29, s11, 0
	global_load_dwordx4 v[2:5], v82, s[22:23]
	v_add_u32_e32 v85, 0x2000, v82
	global_load_dwordx4 v[6:9], v85, s[22:23]
	v_add_u32_e32 v84, 0x4000, v82
	global_load_dwordx4 v[10:13], v84, s[22:23]
	v_add_u32_e32 v85, 0x6000, v82
	global_load_dwordx4 v[14:17], v85, s[22:23]
	v_add_u32_e32 v84, 0x8000, v82
	global_load_dwordx4 v[18:21], v84, s[22:23]
	v_add_u32_e32 v85, 0xa000, v82
	global_load_dwordx4 v[22:25], v85, s[22:23]
	v_add_u32_e32 v84, 0xc000, v82
	global_load_dwordx4 v[26:29], v84, s[22:23]
	v_add_u32_e32 v85, 0xe000, v82
	global_load_dwordx4 v[30:33], v85, s[22:23]
	global_load_dwordx4 v[34:37], v82, s[26:27]
	v_add_u32_e32 v85, 0x2000, v82
	global_load_dwordx4 v[38:41], v85, s[26:27]
	v_add_u32_e32 v84, 0x4000, v82
	global_load_dwordx4 v[42:45], v84, s[26:27]
	v_add_u32_e32 v85, 0x6000, v82
	global_load_dwordx4 v[46:49], v85, s[26:27]
	v_add_u32_e32 v84, 0x8000, v82
	global_load_dwordx4 v[50:53], v84, s[26:27]
	v_add_u32_e32 v85, 0xa000, v82
	global_load_dwordx4 v[54:57], v85, s[26:27]
	v_add_u32_e32 v84, 0xc000, v82
	global_load_dwordx4 v[58:61], v84, s[26:27]
	v_add_u32_e32 v85, 0xe000, v82
	global_load_dwordx4 v[62:65], v85, s[26:27]
	s_waitcnt vmcnt(8)
	v_cvt_pk_bf16_f32 v2, v2, v6
	v_cvt_pk_bf16_f32 v6, v3, v7
	v_cvt_pk_bf16_f32 v66, v4, v8
	v_cvt_pk_bf16_f32 v70, v5, v9
	v_cvt_pk_bf16_f32 v3, v10, v14
	v_cvt_pk_bf16_f32 v7, v11, v15
	v_cvt_pk_bf16_f32 v67, v12, v16
	v_cvt_pk_bf16_f32 v71, v13, v17
	v_cvt_pk_bf16_f32 v4, v18, v22
	v_cvt_pk_bf16_f32 v8, v19, v23
	v_cvt_pk_bf16_f32 v68, v20, v24
	v_cvt_pk_bf16_f32 v72, v21, v25
	v_cvt_pk_bf16_f32 v5, v26, v30
	v_cvt_pk_bf16_f32 v9, v27, v31
	v_cvt_pk_bf16_f32 v69, v28, v32
	v_cvt_pk_bf16_f32 v73, v29, v33
	global_store_dwordx4 v83, v[2:5], s[24:25]
	global_store_dwordx4 v83, v[6:9], s[24:25] offset:128
	global_store_dwordx4 v83, v[66:69], s[24:25] offset:256
	global_store_dwordx4 v83, v[70:73], s[24:25] offset:384
	s_waitcnt vmcnt(4)
	v_cvt_pk_bf16_f32 v34, v34, v38
	v_cvt_pk_bf16_f32 v38, v35, v39
	v_cvt_pk_bf16_f32 v74, v36, v40
	v_cvt_pk_bf16_f32 v78, v37, v41
	v_cvt_pk_bf16_f32 v35, v42, v46
	v_cvt_pk_bf16_f32 v39, v43, v47
	v_cvt_pk_bf16_f32 v75, v44, v48
	v_cvt_pk_bf16_f32 v79, v45, v49
	v_cvt_pk_bf16_f32 v36, v50, v54
	v_cvt_pk_bf16_f32 v40, v51, v55
	v_cvt_pk_bf16_f32 v76, v52, v56
	v_cvt_pk_bf16_f32 v80, v53, v57
	v_cvt_pk_bf16_f32 v37, v58, v62
	v_cvt_pk_bf16_f32 v41, v59, v63
	v_cvt_pk_bf16_f32 v77, v60, v64
	v_cvt_pk_bf16_f32 v81, v61, v65
	global_store_dwordx4 v83, v[34:37], s[28:29]
	global_store_dwordx4 v83, v[38:41], s[28:29] offset:128
	global_store_dwordx4 v83, v[74:77], s[28:29] offset:256
	global_store_dwordx4 v83, v[78:81], s[28:29] offset:384
	s_add_i32 s16, s16, 2
	s_sub_i32 s14, s14, 1
	s_cmp_lg_u32 s14, 0
	s_cbranch_scc1 .Lhost_p8_loop
	s_branch .LBB0_860

.LBB0_1797:
	ds_read_b32 v6, v17 offset:24
	s_waitcnt lgkmcnt(0)
	v_cmp_gt_u32_e64 s[38:39], v6, v2
	s_nop 1
	v_addc_co_u32_e64 v5, s[38:39], 0, v5, s[38:39]
	v_cmp_eq_u32_e64 s[38:39], v6, v2
	s_nop 1
	v_addc_co_u32_e64 v4, s[38:39], 0, v4, s[38:39]
	s_or_b64 exec, exec, s[0:1]
	s_and_saveexec_b64 s[0:1], s[16:17]
	s_cbranch_execnz .LBB0_1739
	s_branch .LBB0_1740
	s_branch .LBB0_1798
.Lhost_p19:
	s_add_i32 s12, s85, 64
	s_lshr_b32 s13, s87, 6
	s_mul_i32 s12, s12, 64
	s_mul_i32 s13, s13, 8
	s_add_i32 s16, s12, s13
	v_readlane_b32 s8, v254, 38
	v_readlane_b32 s9, v254, 39
	v_readlane_b32 s10, v254, 42
	v_readlane_b32 s11, v254, 43
	v_lshrrev_b32_e32 v84, 3, v222
	v_and_b32_e32 v85, 7, v222
	v_lshlrev_b32_e32 v82, 16, v84
	v_lshlrev_b32_e32 v83, 4, v84
	v_lshl_or_b32 v82, v85, 4, v82
	v_lshl_or_b32 v83, v85, 9, v83
	s_add_u32 s10, s10, 0x24c00000
	s_addc_u32 s11, s11, 0
	s_mov_b32 s14, 4
